# moe_cvt: LDS transpose tile laid out as 128-byte rows with XOR-swizzled 16-byte chunks: ds_write_b128 (8 per item) instead of 16 ds_write2_b32, no padding (on top of v34)
# speedup vs baseline: 1.0032x; 1.0032x over previous
.LBB0_1232:
	s_waitcnt vmcnt(0)
	v_mbcnt_lo_u32_b32 v66, -1, 0
	v_mbcnt_hi_u32_b32 v66, -1, v66
	s_waitcnt vmcnt(0)
	v_add_u32_e32 v0, s15, v66
	s_barrier
	v_readfirstlane_b32 s0, v0
	s_ashr_i32 s30, s0, 6
	v_readlane_b32 s0, v253, 52
	s_add_i32 s12, s30, s0
	s_cmp_gt_i32 s12, 0xbfff
	s_cbranch_scc1 .LBB0_1074
	v_and_b32_e32 v119, 7, v66
	v_lshrrev_b32_e32 v120, 3, v66
	s_mulk_i32 s30, 0x2100
	v_lshlrev_b32_e32 v121, 7, v120
	v_xor_b32_e32 v122, 0, v119
	v_lshl_add_u32 v122, v122, 4, v121
	v_add_u32_e32 v122, 0x0, v122
	v_add_u32_e32 v106, s30, v122
	v_xor_b32_e32 v122, 1, v119
	v_lshl_add_u32 v122, v122, 4, v121
	v_add_u32_e32 v122, 0x400, v122
	v_add_u32_e32 v107, s30, v122
	v_xor_b32_e32 v122, 2, v119
	v_lshl_add_u32 v122, v122, 4, v121
	v_add_u32_e32 v122, 0x800, v122
	v_add_u32_e32 v108, s30, v122
	v_xor_b32_e32 v122, 3, v119
	v_lshl_add_u32 v122, v122, 4, v121
	v_add_u32_e32 v122, 0xc00, v122
	v_add_u32_e32 v109, s30, v122
	v_xor_b32_e32 v122, 4, v119
	v_lshl_add_u32 v122, v122, 4, v121
	v_add_u32_e32 v122, 0x1000, v122
	v_add_u32_e32 v110, s30, v122
	v_xor_b32_e32 v122, 5, v119
	v_lshl_add_u32 v122, v122, 4, v121
	v_add_u32_e32 v122, 0x1400, v122
	v_add_u32_e32 v111, s30, v122
	v_xor_b32_e32 v122, 6, v119
	v_lshl_add_u32 v122, v122, 4, v121
	v_add_u32_e32 v122, 0x1800, v122
	v_add_u32_e32 v112, s30, v122
	v_xor_b32_e32 v122, 7, v119
	v_lshl_add_u32 v122, v122, 4, v121
	v_add_u32_e32 v122, 0x1c00, v122
	v_add_u32_e32 v113, s30, v122
	v_lshrrev_b32_e32 v121, 2, v120
	v_and_b32_e32 v0, 3, v120
	v_add_u32_e32 v122, 0, v121
	v_xor_b32_e32 v122, v122, v119
	v_lshl_add_u32 v122, v122, 2, v0
	v_lshlrev_b32_e32 v122, 2, v122
	v_lshl_add_u32 v122, v119, 10, v122
	v_add_u32_e32 v114, s30, v122
	v_add_u32_e32 v122, 2, v121
	v_xor_b32_e32 v122, v122, v119
	v_lshl_add_u32 v122, v122, 2, v0
	v_lshlrev_b32_e32 v122, 2, v122
	v_lshl_add_u32 v122, v119, 10, v122
	v_add_u32_e32 v188, s30, v122
	v_add_u32_e32 v122, 4, v121
	v_xor_b32_e32 v122, v122, v119
	v_lshl_add_u32 v122, v122, 2, v0
	v_lshlrev_b32_e32 v122, 2, v122
	v_lshl_add_u32 v122, v119, 10, v122
	v_add_u32_e32 v189, s30, v122
	v_add_u32_e32 v122, 6, v121
	v_xor_b32_e32 v122, v122, v119
	v_lshl_add_u32 v122, v122, 2, v0
	v_lshlrev_b32_e32 v122, 2, v122
	v_lshl_add_u32 v122, v119, 10, v122
	v_add_u32_e32 v190, s30, v122
	s_mov_b32 s26, 0x42800000
	s_mov_b32 s27, 0x42800000
	s_mov_b32 s13, 0x1000000
	s_mov_b32 s23, 0x400000
	s_mov_b32 s29, 0
	s_lshr_b32 s0, s12, 10
	s_add_i32 s0, s0, s46
	s_mov_b32 s1, 0
	v_readlane_b32 s34, v254, 29
	v_readlane_b32 s35, v254, 30
	s_lshl_b64 s[36:37], s[0:1], 23
	s_add_u32 s6, s34, s36
	s_addc_u32 s7, s35, s37
	s_bfe_u32 s31, s12, 0x40006
	s_lshl_b32 s36, s31, 19
	s_add_u32 s6, s6, s36
	s_addc_u32 s7, s7, 0
	s_and_b32 s38, s12, 63
	s_lshl_b32 s36, s38, 7
	s_add_u32 s6, s6, s36
	s_addc_u32 s7, s7, 0
	s_lshl_b64 s[36:37], s[0:1], 21
	s_add_u32 s8, s49, s36
	s_addc_u32 s9, s50, s37
	s_lshl_b32 s36, s38, 15
	s_add_u32 s8, s8, s36
	s_addc_u32 s9, s9, 0
	s_lshl_b32 s36, s31, 6
	s_add_u32 s8, s8, s36
	s_addc_u32 s9, s9, 0
	s_mov_b32 s10, 16
	v_lshlrev_b32_e32 v121, 13, v120
	v_lshl_add_u32 v98, v119, 4, v121
	v_add_u32_e32 v99, 0x10000, v98
	v_add_u32_e32 v100, 0x20000, v98
	v_add_u32_e32 v101, 0x30000, v98
	v_add_u32_e32 v102, 0x40000, v98
	v_add_u32_e32 v103, 0x50000, v98
	v_add_u32_e32 v104, 0x60000, v98
	v_add_u32_e32 v105, 0x70000, v98
	v_and_b32_e32 v121, 1, v120
	v_lshlrev_b32_e32 v121, 2, v121
	v_lshrrev_b32_e32 v122, 1, v120
	v_or_b32_e32 v121, v121, v122
	v_lshlrev_b32_e32 v121, 10, v121
	v_lshl_add_u32 v115, v119, 3, v121
	v_add_u32_e32 v116, 0x2000, v115
	v_add_u32_e32 v117, 0x4000, v115
	v_add_u32_e32 v118, 0x6000, v115
	s_branch .Lcvt_run

.Lcvt_loop:
	global_load_dwordx4 v[156:159], v98, s[6:7]
	global_load_dwordx4 v[160:163], v99, s[6:7]
	global_load_dwordx4 v[164:167], v100, s[6:7]
	global_load_dwordx4 v[168:171], v101, s[6:7]
	global_load_dwordx4 v[172:175], v102, s[6:7]
	global_load_dwordx4 v[176:179], v103, s[6:7]
	global_load_dwordx4 v[180:183], v104, s[6:7]
	global_load_dwordx4 v[184:187], v105, s[6:7]
	s_cmp_lg_u32 s11, 0
	s_cselect_b32 s0, s13, 0
	s_cselect_b32 s1, 1, 0
	s_add_u32 s6, s6, s0
	s_addc_u32 s7, s7, 0
	s_sub_u32 s11, s11, s1
	s_waitcnt vmcnt(32)
	ds_write_b128 v106, v[2:5]
	ds_write_b128 v107, v[6:9]
	ds_write_b128 v108, v[10:13]
	ds_write_b128 v109, v[14:17]
	ds_write_b128 v110, v[18:21]
	ds_write_b128 v111, v[22:25]
	ds_write_b128 v112, v[26:29]
	ds_write_b128 v113, v[30:33]
	s_waitcnt lgkmcnt(0)
	ds_read2_b32 v[2:3], v114 offset1:32
	ds_read2_b32 v[4:5], v114 offset0:64 offset1:96
	ds_read2_b32 v[6:7], v114 offset0:128 offset1:160
	ds_read2_b32 v[8:9], v114 offset0:192 offset1:224
	ds_read2_b32 v[10:11], v188 offset1:32
	ds_read2_b32 v[12:13], v188 offset0:64 offset1:96
	ds_read2_b32 v[14:15], v188 offset0:128 offset1:160
	ds_read2_b32 v[16:17], v188 offset0:192 offset1:224
	ds_read2_b32 v[18:19], v189 offset1:32
	ds_read2_b32 v[20:21], v189 offset0:64 offset1:96
	ds_read2_b32 v[22:23], v189 offset0:128 offset1:160
	ds_read2_b32 v[24:25], v189 offset0:192 offset1:224
	ds_read2_b32 v[26:27], v190 offset1:32
	ds_read2_b32 v[28:29], v190 offset0:64 offset1:96
	ds_read2_b32 v[30:31], v190 offset0:128 offset1:160
	ds_read2_b32 v[32:33], v190 offset0:192 offset1:224
	s_waitcnt lgkmcnt(12)
	v_pk_mul_f32 v[2:3], v[2:3], s[26:27] op_sel_hi:[1,0]
	v_pk_mul_f32 v[4:5], v[4:5], s[26:27] op_sel_hi:[1,0]
	v_pk_mul_f32 v[6:7], v[6:7], s[26:27] op_sel_hi:[1,0]
	v_pk_mul_f32 v[8:9], v[8:9], s[26:27] op_sel_hi:[1,0]
	v_cvt_pk_fp8_f32 v2, v2, v3
	v_cvt_pk_fp8_f32 v3, v6, v7
	v_cvt_pk_fp8_f32 v2, v4, v5 op_sel:[0,0,1]
	v_cvt_pk_fp8_f32 v3, v8, v9 op_sel:[0,0,1]
	s_nop 1
	global_store_dwordx2 v115, v[2:3], s[8:9]
	s_waitcnt lgkmcnt(8)
	v_pk_mul_f32 v[10:11], v[10:11], s[26:27] op_sel_hi:[1,0]
	v_pk_mul_f32 v[12:13], v[12:13], s[26:27] op_sel_hi:[1,0]
	v_pk_mul_f32 v[14:15], v[14:15], s[26:27] op_sel_hi:[1,0]
	v_pk_mul_f32 v[16:17], v[16:17], s[26:27] op_sel_hi:[1,0]
	v_cvt_pk_fp8_f32 v10, v10, v11
	v_cvt_pk_fp8_f32 v11, v14, v15
	v_cvt_pk_fp8_f32 v10, v12, v13 op_sel:[0,0,1]
	v_cvt_pk_fp8_f32 v11, v16, v17 op_sel:[0,0,1]
	s_nop 1
	global_store_dwordx2 v116, v[10:11], s[8:9]
	s_waitcnt lgkmcnt(4)
	v_pk_mul_f32 v[18:19], v[18:19], s[26:27] op_sel_hi:[1,0]
	v_pk_mul_f32 v[20:21], v[20:21], s[26:27] op_sel_hi:[1,0]
	v_pk_mul_f32 v[22:23], v[22:23], s[26:27] op_sel_hi:[1,0]
	v_pk_mul_f32 v[24:25], v[24:25], s[26:27] op_sel_hi:[1,0]
	v_cvt_pk_fp8_f32 v18, v18, v19
	v_cvt_pk_fp8_f32 v19, v22, v23
	v_cvt_pk_fp8_f32 v18, v20, v21 op_sel:[0,0,1]
	v_cvt_pk_fp8_f32 v19, v24, v25 op_sel:[0,0,1]
	s_nop 1
	global_store_dwordx2 v117, v[18:19], s[8:9]
	s_waitcnt lgkmcnt(0)
	v_pk_mul_f32 v[26:27], v[26:27], s[26:27] op_sel_hi:[1,0]
	v_pk_mul_f32 v[28:29], v[28:29], s[26:27] op_sel_hi:[1,0]
	v_pk_mul_f32 v[30:31], v[30:31], s[26:27] op_sel_hi:[1,0]
	v_pk_mul_f32 v[32:33], v[32:33], s[26:27] op_sel_hi:[1,0]
	v_cvt_pk_fp8_f32 v26, v26, v27
	v_cvt_pk_fp8_f32 v27, v30, v31
	v_cvt_pk_fp8_f32 v26, v28, v29 op_sel:[0,0,1]
	v_cvt_pk_fp8_f32 v27, v32, v33 op_sel:[0,0,1]
	s_nop 1
	global_store_dwordx2 v118, v[26:27], s[8:9]
	s_add_u32 s8, s8, s23
	s_addc_u32 s9, s9, 0
	s_add_i32 s10, s10, -1
	s_cmp_eq_u32 s10, 0
	s_cbranch_scc1 .Lcvt_phase_done
	global_load_dwordx4 v[2:5], v98, s[6:7]
	global_load_dwordx4 v[6:9], v99, s[6:7]
	global_load_dwordx4 v[10:13], v100, s[6:7]
	global_load_dwordx4 v[14:17], v101, s[6:7]
	global_load_dwordx4 v[18:21], v102, s[6:7]
	global_load_dwordx4 v[22:25], v103, s[6:7]
	global_load_dwordx4 v[26:29], v104, s[6:7]
	global_load_dwordx4 v[30:33], v105, s[6:7]
	s_cmp_lg_u32 s11, 0
	s_cselect_b32 s0, s13, 0
	s_cselect_b32 s1, 1, 0
	s_add_u32 s6, s6, s0
	s_addc_u32 s7, s7, 0
	s_sub_u32 s11, s11, s1
	s_waitcnt vmcnt(32)
	ds_write_b128 v106, v[34:37]
	ds_write_b128 v107, v[38:41]
	ds_write_b128 v108, v[42:45]
	ds_write_b128 v109, v[46:49]
	ds_write_b128 v110, v[50:53]
	ds_write_b128 v111, v[54:57]
	ds_write_b128 v112, v[58:61]
	ds_write_b128 v113, v[62:65]
	s_waitcnt lgkmcnt(0)
	ds_read2_b32 v[34:35], v114 offset1:32
	ds_read2_b32 v[36:37], v114 offset0:64 offset1:96
	ds_read2_b32 v[38:39], v114 offset0:128 offset1:160
	ds_read2_b32 v[40:41], v114 offset0:192 offset1:224
	ds_read2_b32 v[42:43], v188 offset1:32
	ds_read2_b32 v[44:45], v188 offset0:64 offset1:96
	ds_read2_b32 v[46:47], v188 offset0:128 offset1:160
	ds_read2_b32 v[48:49], v188 offset0:192 offset1:224
	ds_read2_b32 v[50:51], v189 offset1:32
	ds_read2_b32 v[52:53], v189 offset0:64 offset1:96
	ds_read2_b32 v[54:55], v189 offset0:128 offset1:160
	ds_read2_b32 v[56:57], v189 offset0:192 offset1:224
	ds_read2_b32 v[58:59], v190 offset1:32
	ds_read2_b32 v[60:61], v190 offset0:64 offset1:96
	ds_read2_b32 v[62:63], v190 offset0:128 offset1:160
	ds_read2_b32 v[64:65], v190 offset0:192 offset1:224
	s_waitcnt lgkmcnt(12)
	v_pk_mul_f32 v[34:35], v[34:35], s[26:27] op_sel_hi:[1,0]
	v_pk_mul_f32 v[36:37], v[36:37], s[26:27] op_sel_hi:[1,0]
	v_pk_mul_f32 v[38:39], v[38:39], s[26:27] op_sel_hi:[1,0]
	v_pk_mul_f32 v[40:41], v[40:41], s[26:27] op_sel_hi:[1,0]
	v_cvt_pk_fp8_f32 v34, v34, v35
	v_cvt_pk_fp8_f32 v35, v38, v39
	v_cvt_pk_fp8_f32 v34, v36, v37 op_sel:[0,0,1]
	v_cvt_pk_fp8_f32 v35, v40, v41 op_sel:[0,0,1]
	s_nop 1
	global_store_dwordx2 v115, v[34:35], s[8:9]
	s_waitcnt lgkmcnt(8)
	v_pk_mul_f32 v[42:43], v[42:43], s[26:27] op_sel_hi:[1,0]
	v_pk_mul_f32 v[44:45], v[44:45], s[26:27] op_sel_hi:[1,0]
	v_pk_mul_f32 v[46:47], v[46:47], s[26:27] op_sel_hi:[1,0]
	v_pk_mul_f32 v[48:49], v[48:49], s[26:27] op_sel_hi:[1,0]
	v_cvt_pk_fp8_f32 v42, v42, v43
	v_cvt_pk_fp8_f32 v43, v46, v47
	v_cvt_pk_fp8_f32 v42, v44, v45 op_sel:[0,0,1]
	v_cvt_pk_fp8_f32 v43, v48, v49 op_sel:[0,0,1]
	s_nop 1
	global_store_dwordx2 v116, v[42:43], s[8:9]
	s_waitcnt lgkmcnt(4)
	v_pk_mul_f32 v[50:51], v[50:51], s[26:27] op_sel_hi:[1,0]
	v_pk_mul_f32 v[52:53], v[52:53], s[26:27] op_sel_hi:[1,0]
	v_pk_mul_f32 v[54:55], v[54:55], s[26:27] op_sel_hi:[1,0]
	v_pk_mul_f32 v[56:57], v[56:57], s[26:27] op_sel_hi:[1,0]
	v_cvt_pk_fp8_f32 v50, v50, v51
	v_cvt_pk_fp8_f32 v51, v54, v55
	v_cvt_pk_fp8_f32 v50, v52, v53 op_sel:[0,0,1]
	v_cvt_pk_fp8_f32 v51, v56, v57 op_sel:[0,0,1]
	s_nop 1
	global_store_dwordx2 v117, v[50:51], s[8:9]
	s_waitcnt lgkmcnt(0)
	v_pk_mul_f32 v[58:59], v[58:59], s[26:27] op_sel_hi:[1,0]
	v_pk_mul_f32 v[60:61], v[60:61], s[26:27] op_sel_hi:[1,0]
	v_pk_mul_f32 v[62:63], v[62:63], s[26:27] op_sel_hi:[1,0]
	v_pk_mul_f32 v[64:65], v[64:65], s[26:27] op_sel_hi:[1,0]
	v_cvt_pk_fp8_f32 v58, v58, v59
	v_cvt_pk_fp8_f32 v59, v62, v63
	v_cvt_pk_fp8_f32 v58, v60, v61 op_sel:[0,0,1]
	v_cvt_pk_fp8_f32 v59, v64, v65 op_sel:[0,0,1]
	s_nop 1
	global_store_dwordx2 v118, v[58:59], s[8:9]
	s_add_u32 s8, s8, s23
	s_addc_u32 s9, s9, 0
	s_add_i32 s10, s10, -1
	s_cmp_eq_u32 s10, 0
	s_cbranch_scc1 .Lcvt_phase_done
	global_load_dwordx4 v[34:37], v98, s[6:7]
	global_load_dwordx4 v[38:41], v99, s[6:7]
	global_load_dwordx4 v[42:45], v100, s[6:7]
	global_load_dwordx4 v[46:49], v101, s[6:7]
	global_load_dwordx4 v[50:53], v102, s[6:7]
	global_load_dwordx4 v[54:57], v103, s[6:7]
	global_load_dwordx4 v[58:61], v104, s[6:7]
	global_load_dwordx4 v[62:65], v105, s[6:7]
	s_cmp_lg_u32 s11, 0
	s_cselect_b32 s0, s13, 0
	s_cselect_b32 s1, 1, 0
	s_add_u32 s6, s6, s0
	s_addc_u32 s7, s7, 0
	s_sub_u32 s11, s11, s1
	s_waitcnt vmcnt(32)
	ds_write_b128 v106, v[66:69]
	ds_write_b128 v107, v[70:73]
	ds_write_b128 v108, v[74:77]
	ds_write_b128 v109, v[78:81]
	ds_write_b128 v110, v[82:85]
	ds_write_b128 v111, v[86:89]
	ds_write_b128 v112, v[90:93]
	ds_write_b128 v113, v[94:97]
	s_waitcnt lgkmcnt(0)
	ds_read2_b32 v[66:67], v114 offset1:32
	ds_read2_b32 v[68:69], v114 offset0:64 offset1:96
	ds_read2_b32 v[70:71], v114 offset0:128 offset1:160
	ds_read2_b32 v[72:73], v114 offset0:192 offset1:224
	ds_read2_b32 v[74:75], v188 offset1:32
	ds_read2_b32 v[76:77], v188 offset0:64 offset1:96
	ds_read2_b32 v[78:79], v188 offset0:128 offset1:160
	ds_read2_b32 v[80:81], v188 offset0:192 offset1:224
	ds_read2_b32 v[82:83], v189 offset1:32
	ds_read2_b32 v[84:85], v189 offset0:64 offset1:96
	ds_read2_b32 v[86:87], v189 offset0:128 offset1:160
	ds_read2_b32 v[88:89], v189 offset0:192 offset1:224
	ds_read2_b32 v[90:91], v190 offset1:32
	ds_read2_b32 v[92:93], v190 offset0:64 offset1:96
	ds_read2_b32 v[94:95], v190 offset0:128 offset1:160
	ds_read2_b32 v[96:97], v190 offset0:192 offset1:224
	s_waitcnt lgkmcnt(12)
	v_pk_mul_f32 v[66:67], v[66:67], s[26:27] op_sel_hi:[1,0]
	v_pk_mul_f32 v[68:69], v[68:69], s[26:27] op_sel_hi:[1,0]
	v_pk_mul_f32 v[70:71], v[70:71], s[26:27] op_sel_hi:[1,0]
	v_pk_mul_f32 v[72:73], v[72:73], s[26:27] op_sel_hi:[1,0]
	v_cvt_pk_fp8_f32 v66, v66, v67
	v_cvt_pk_fp8_f32 v67, v70, v71
	v_cvt_pk_fp8_f32 v66, v68, v69 op_sel:[0,0,1]
	v_cvt_pk_fp8_f32 v67, v72, v73 op_sel:[0,0,1]
	s_nop 1
	global_store_dwordx2 v115, v[66:67], s[8:9]
	s_waitcnt lgkmcnt(8)
	v_pk_mul_f32 v[74:75], v[74:75], s[26:27] op_sel_hi:[1,0]
	v_pk_mul_f32 v[76:77], v[76:77], s[26:27] op_sel_hi:[1,0]
	v_pk_mul_f32 v[78:79], v[78:79], s[26:27] op_sel_hi:[1,0]
	v_pk_mul_f32 v[80:81], v[80:81], s[26:27] op_sel_hi:[1,0]
	v_cvt_pk_fp8_f32 v74, v74, v75
	v_cvt_pk_fp8_f32 v75, v78, v79
	v_cvt_pk_fp8_f32 v74, v76, v77 op_sel:[0,0,1]
	v_cvt_pk_fp8_f32 v75, v80, v81 op_sel:[0,0,1]
	s_nop 1
	global_store_dwordx2 v116, v[74:75], s[8:9]
	s_waitcnt lgkmcnt(4)
	v_pk_mul_f32 v[82:83], v[82:83], s[26:27] op_sel_hi:[1,0]
	v_pk_mul_f32 v[84:85], v[84:85], s[26:27] op_sel_hi:[1,0]
	v_pk_mul_f32 v[86:87], v[86:87], s[26:27] op_sel_hi:[1,0]
	v_pk_mul_f32 v[88:89], v[88:89], s[26:27] op_sel_hi:[1,0]
	v_cvt_pk_fp8_f32 v82, v82, v83
	v_cvt_pk_fp8_f32 v83, v86, v87
	v_cvt_pk_fp8_f32 v82, v84, v85 op_sel:[0,0,1]
	v_cvt_pk_fp8_f32 v83, v88, v89 op_sel:[0,0,1]
	s_nop 1
	global_store_dwordx2 v117, v[82:83], s[8:9]
	s_waitcnt lgkmcnt(0)
	v_pk_mul_f32 v[90:91], v[90:91], s[26:27] op_sel_hi:[1,0]
	v_pk_mul_f32 v[92:93], v[92:93], s[26:27] op_sel_hi:[1,0]
	v_pk_mul_f32 v[94:95], v[94:95], s[26:27] op_sel_hi:[1,0]
	v_pk_mul_f32 v[96:97], v[96:97], s[26:27] op_sel_hi:[1,0]
	v_cvt_pk_fp8_f32 v90, v90, v91
	v_cvt_pk_fp8_f32 v91, v94, v95
	v_cvt_pk_fp8_f32 v90, v92, v93 op_sel:[0,0,1]
	v_cvt_pk_fp8_f32 v91, v96, v97 op_sel:[0,0,1]
	s_nop 1
	global_store_dwordx2 v118, v[90:91], s[8:9]
	s_add_u32 s8, s8, s23
	s_addc_u32 s9, s9, 0
	s_add_i32 s10, s10, -1
	s_cmp_eq_u32 s10, 0
	s_cbranch_scc1 .Lcvt_phase_done
	global_load_dwordx4 v[66:69], v98, s[6:7]
	global_load_dwordx4 v[70:73], v99, s[6:7]
	global_load_dwordx4 v[74:77], v100, s[6:7]
	global_load_dwordx4 v[78:81], v101, s[6:7]
	global_load_dwordx4 v[82:85], v102, s[6:7]
	global_load_dwordx4 v[86:89], v103, s[6:7]
	global_load_dwordx4 v[90:93], v104, s[6:7]
	global_load_dwordx4 v[94:97], v105, s[6:7]
	s_cmp_lg_u32 s11, 0
	s_cselect_b32 s0, s13, 0
	s_cselect_b32 s1, 1, 0
	s_add_u32 s6, s6, s0
	s_addc_u32 s7, s7, 0
	s_sub_u32 s11, s11, s1
	s_waitcnt vmcnt(32)
	ds_write_b128 v106, v[124:127]
	ds_write_b128 v107, v[128:131]
	ds_write_b128 v108, v[132:135]
	ds_write_b128 v109, v[136:139]
	ds_write_b128 v110, v[140:143]
	ds_write_b128 v111, v[144:147]
	ds_write_b128 v112, v[148:151]
	ds_write_b128 v113, v[152:155]
	s_waitcnt lgkmcnt(0)
	ds_read2_b32 v[124:125], v114 offset1:32
	ds_read2_b32 v[126:127], v114 offset0:64 offset1:96
	ds_read2_b32 v[128:129], v114 offset0:128 offset1:160
	ds_read2_b32 v[130:131], v114 offset0:192 offset1:224
	ds_read2_b32 v[132:133], v188 offset1:32
	ds_read2_b32 v[134:135], v188 offset0:64 offset1:96
	ds_read2_b32 v[136:137], v188 offset0:128 offset1:160
	ds_read2_b32 v[138:139], v188 offset0:192 offset1:224
	ds_read2_b32 v[140:141], v189 offset1:32
	ds_read2_b32 v[142:143], v189 offset0:64 offset1:96
	ds_read2_b32 v[144:145], v189 offset0:128 offset1:160
	ds_read2_b32 v[146:147], v189 offset0:192 offset1:224
	ds_read2_b32 v[148:149], v190 offset1:32
	ds_read2_b32 v[150:151], v190 offset0:64 offset1:96
	ds_read2_b32 v[152:153], v190 offset0:128 offset1:160
	ds_read2_b32 v[154:155], v190 offset0:192 offset1:224
	s_waitcnt lgkmcnt(12)
	v_pk_mul_f32 v[124:125], v[124:125], s[26:27] op_sel_hi:[1,0]
	v_pk_mul_f32 v[126:127], v[126:127], s[26:27] op_sel_hi:[1,0]
	v_pk_mul_f32 v[128:129], v[128:129], s[26:27] op_sel_hi:[1,0]
	v_pk_mul_f32 v[130:131], v[130:131], s[26:27] op_sel_hi:[1,0]
	v_cvt_pk_fp8_f32 v124, v124, v125
	v_cvt_pk_fp8_f32 v125, v128, v129
	v_cvt_pk_fp8_f32 v124, v126, v127 op_sel:[0,0,1]
	v_cvt_pk_fp8_f32 v125, v130, v131 op_sel:[0,0,1]
	s_nop 1
	global_store_dwordx2 v115, v[124:125], s[8:9]
	s_waitcnt lgkmcnt(8)
	v_pk_mul_f32 v[132:133], v[132:133], s[26:27] op_sel_hi:[1,0]
	v_pk_mul_f32 v[134:135], v[134:135], s[26:27] op_sel_hi:[1,0]
	v_pk_mul_f32 v[136:137], v[136:137], s[26:27] op_sel_hi:[1,0]
	v_pk_mul_f32 v[138:139], v[138:139], s[26:27] op_sel_hi:[1,0]
	v_cvt_pk_fp8_f32 v132, v132, v133
	v_cvt_pk_fp8_f32 v133, v136, v137
	v_cvt_pk_fp8_f32 v132, v134, v135 op_sel:[0,0,1]
	v_cvt_pk_fp8_f32 v133, v138, v139 op_sel:[0,0,1]
	s_nop 1
	global_store_dwordx2 v116, v[132:133], s[8:9]
	s_waitcnt lgkmcnt(4)
	v_pk_mul_f32 v[140:141], v[140:141], s[26:27] op_sel_hi:[1,0]
	v_pk_mul_f32 v[142:143], v[142:143], s[26:27] op_sel_hi:[1,0]
	v_pk_mul_f32 v[144:145], v[144:145], s[26:27] op_sel_hi:[1,0]
	v_pk_mul_f32 v[146:147], v[146:147], s[26:27] op_sel_hi:[1,0]
	v_cvt_pk_fp8_f32 v140, v140, v141
	v_cvt_pk_fp8_f32 v141, v144, v145
	v_cvt_pk_fp8_f32 v140, v142, v143 op_sel:[0,0,1]
	v_cvt_pk_fp8_f32 v141, v146, v147 op_sel:[0,0,1]
	s_nop 1
	global_store_dwordx2 v117, v[140:141], s[8:9]
	s_waitcnt lgkmcnt(0)
	v_pk_mul_f32 v[148:149], v[148:149], s[26:27] op_sel_hi:[1,0]
	v_pk_mul_f32 v[150:151], v[150:151], s[26:27] op_sel_hi:[1,0]
	v_pk_mul_f32 v[152:153], v[152:153], s[26:27] op_sel_hi:[1,0]
	v_pk_mul_f32 v[154:155], v[154:155], s[26:27] op_sel_hi:[1,0]
	v_cvt_pk_fp8_f32 v148, v148, v149
	v_cvt_pk_fp8_f32 v149, v152, v153
	v_cvt_pk_fp8_f32 v148, v150, v151 op_sel:[0,0,1]
	v_cvt_pk_fp8_f32 v149, v154, v155 op_sel:[0,0,1]
	s_nop 1
	global_store_dwordx2 v118, v[148:149], s[8:9]
	s_add_u32 s8, s8, s23
	s_addc_u32 s9, s9, 0
	s_add_i32 s10, s10, -1
	s_cmp_eq_u32 s10, 0
	s_cbranch_scc1 .Lcvt_phase_done
	global_load_dwordx4 v[124:127], v98, s[6:7]
	global_load_dwordx4 v[128:131], v99, s[6:7]
	global_load_dwordx4 v[132:135], v100, s[6:7]
	global_load_dwordx4 v[136:139], v101, s[6:7]
	global_load_dwordx4 v[140:143], v102, s[6:7]
	global_load_dwordx4 v[144:147], v103, s[6:7]
	global_load_dwordx4 v[148:151], v104, s[6:7]
	global_load_dwordx4 v[152:155], v105, s[6:7]
	s_cmp_lg_u32 s11, 0
	s_cselect_b32 s0, s13, 0
	s_cselect_b32 s1, 1, 0
	s_add_u32 s6, s6, s0
	s_addc_u32 s7, s7, 0
	s_sub_u32 s11, s11, s1
	s_waitcnt vmcnt(32)
	ds_write_b128 v106, v[156:159]
	ds_write_b128 v107, v[160:163]
	ds_write_b128 v108, v[164:167]
	ds_write_b128 v109, v[168:171]
	ds_write_b128 v110, v[172:175]
	ds_write_b128 v111, v[176:179]
	ds_write_b128 v112, v[180:183]
	ds_write_b128 v113, v[184:187]
	s_waitcnt lgkmcnt(0)
	ds_read2_b32 v[156:157], v114 offset1:32
	ds_read2_b32 v[158:159], v114 offset0:64 offset1:96
	ds_read2_b32 v[160:161], v114 offset0:128 offset1:160
	ds_read2_b32 v[162:163], v114 offset0:192 offset1:224
	ds_read2_b32 v[164:165], v188 offset1:32
	ds_read2_b32 v[166:167], v188 offset0:64 offset1:96
	ds_read2_b32 v[168:169], v188 offset0:128 offset1:160
	ds_read2_b32 v[170:171], v188 offset0:192 offset1:224
	ds_read2_b32 v[172:173], v189 offset1:32
	ds_read2_b32 v[174:175], v189 offset0:64 offset1:96
	ds_read2_b32 v[176:177], v189 offset0:128 offset1:160
	ds_read2_b32 v[178:179], v189 offset0:192 offset1:224
	ds_read2_b32 v[180:181], v190 offset1:32
	ds_read2_b32 v[182:183], v190 offset0:64 offset1:96
	ds_read2_b32 v[184:185], v190 offset0:128 offset1:160
	ds_read2_b32 v[186:187], v190 offset0:192 offset1:224
	s_waitcnt lgkmcnt(12)
	v_pk_mul_f32 v[156:157], v[156:157], s[26:27] op_sel_hi:[1,0]
	v_pk_mul_f32 v[158:159], v[158:159], s[26:27] op_sel_hi:[1,0]
	v_pk_mul_f32 v[160:161], v[160:161], s[26:27] op_sel_hi:[1,0]
	v_pk_mul_f32 v[162:163], v[162:163], s[26:27] op_sel_hi:[1,0]
	v_cvt_pk_fp8_f32 v156, v156, v157
	v_cvt_pk_fp8_f32 v157, v160, v161
	v_cvt_pk_fp8_f32 v156, v158, v159 op_sel:[0,0,1]
	v_cvt_pk_fp8_f32 v157, v162, v163 op_sel:[0,0,1]
	s_nop 1
	global_store_dwordx2 v115, v[156:157], s[8:9]
	s_waitcnt lgkmcnt(8)
	v_pk_mul_f32 v[164:165], v[164:165], s[26:27] op_sel_hi:[1,0]
	v_pk_mul_f32 v[166:167], v[166:167], s[26:27] op_sel_hi:[1,0]
	v_pk_mul_f32 v[168:169], v[168:169], s[26:27] op_sel_hi:[1,0]
	v_pk_mul_f32 v[170:171], v[170:171], s[26:27] op_sel_hi:[1,0]
	v_cvt_pk_fp8_f32 v164, v164, v165
	v_cvt_pk_fp8_f32 v165, v168, v169
	v_cvt_pk_fp8_f32 v164, v166, v167 op_sel:[0,0,1]
	v_cvt_pk_fp8_f32 v165, v170, v171 op_sel:[0,0,1]
	s_nop 1
	global_store_dwordx2 v116, v[164:165], s[8:9]
	s_waitcnt lgkmcnt(4)
	v_pk_mul_f32 v[172:173], v[172:173], s[26:27] op_sel_hi:[1,0]
	v_pk_mul_f32 v[174:175], v[174:175], s[26:27] op_sel_hi:[1,0]
	v_pk_mul_f32 v[176:177], v[176:177], s[26:27] op_sel_hi:[1,0]
	v_pk_mul_f32 v[178:179], v[178:179], s[26:27] op_sel_hi:[1,0]
	v_cvt_pk_fp8_f32 v172, v172, v173
	v_cvt_pk_fp8_f32 v173, v176, v177
	v_cvt_pk_fp8_f32 v172, v174, v175 op_sel:[0,0,1]
	v_cvt_pk_fp8_f32 v173, v178, v179 op_sel:[0,0,1]
	s_nop 1
	global_store_dwordx2 v117, v[172:173], s[8:9]
	s_waitcnt lgkmcnt(0)
	v_pk_mul_f32 v[180:181], v[180:181], s[26:27] op_sel_hi:[1,0]
	v_pk_mul_f32 v[182:183], v[182:183], s[26:27] op_sel_hi:[1,0]
	v_pk_mul_f32 v[184:185], v[184:185], s[26:27] op_sel_hi:[1,0]
	v_pk_mul_f32 v[186:187], v[186:187], s[26:27] op_sel_hi:[1,0]
	v_cvt_pk_fp8_f32 v180, v180, v181
	v_cvt_pk_fp8_f32 v181, v184, v185
	v_cvt_pk_fp8_f32 v180, v182, v183 op_sel:[0,0,1]
	v_cvt_pk_fp8_f32 v181, v186, v187 op_sel:[0,0,1]
	s_nop 1
	global_store_dwordx2 v118, v[180:181], s[8:9]
	s_add_u32 s8, s8, s23
	s_addc_u32 s9, s9, 0
	s_add_i32 s10, s10, -1
	s_cmp_eq_u32 s10, 0
	s_cbranch_scc1 .Lcvt_phase_done
	s_branch .Lcvt_loop
